# speedup vs baseline: 1.0107x; 1.0106x over previous
_Z10k_transferPKtS0_PKfPKiS2_S4_PfS5_S5_:
	s_load_dwordx4 s[16:19], s[0:1], 0x18
	s_load_dwordx2 s[14:15], s[0:1], 0x28
	s_mov_b64 s[4:5], -1
	s_cmpk_gt_i32 s2, 0x3ff
	v_cmp_gt_u32_e64 s[10:11], 64, v0
	s_cbranch_scc0 .LBB3_31
	s_cmpk_gt_u32 s2, 0x7ff
	s_cbranch_scc0 .LBB3_14
	s_add_i32 s12, s2, 0xfffff800
	s_lshr_b32 s3, s12, 4
	s_lshl_b32 s8, s3, 3
	s_load_dwordx2 s[4:5], s[0:1], 0x0
	s_waitcnt lgkmcnt(0)
	s_load_dwordx2 s[6:7], s[14:15], s8 offset:0x0
	s_and_saveexec_b64 s[8:9], s[10:11]
	s_cbranch_execz .LBB3_4
	v_lshl_or_b32 v2, s3, 6, v0
	v_mov_b32_e32 v3, 0
	v_lshlrev_b64 v[2:3], 2, v[2:3]
	v_lshl_add_u64 v[4:5], s[16:17], 0, v[2:3]
	v_lshl_add_u64 v[2:3], s[18:19], 0, v[2:3]
	global_load_dword v49, v[4:5], off
	global_load_dword v50, v[2:3], off
	v_lshlrev_b32_e32 v51, 2, v0
	v_add_u32_e32 v51, 0x50, v51

.LBB3_10:
	s_or_b64 exec, exec, s[4:5]
	s_and_saveexec_b64 s[4:5], s[10:11]
	s_waitcnt vmcnt(0)
	ds_write2st64_b32 v51, v49, v50 offset0:70 offset1:71
	s_or_b64 exec, exec, s[4:5]
	s_movk_i32 s4, 0x200
	v_cmp_gt_u32_e32 vcc, s4, v0
	s_waitcnt lgkmcnt(0)
	s_barrier
	s_and_saveexec_b64 s[22:23], vcc
	s_cbranch_execz .LBB3_13
	v_and_b32_e32 v1, 7, v0
	v_add_u32_e32 v15, 1, v1
	v_lshrrev_b32_e32 v5, 5, v0
	s_waitcnt vmcnt(0)
	v_min_u32_e32 v3, 7, v15
	v_add_u32_e32 v10, 1, v5
	v_lshlrev_b32_e32 v9, 2, v3
	v_add_u32_e32 v3, -1, v1
	v_min_u32_e32 v4, 7, v10
	v_mov_b32_e32 v7, 0x4650
	v_max_i32_e32 v13, 0, v3
	v_lshl_add_u32 v4, v4, 5, v7
	v_lshlrev_b32_e32 v6, 2, v1
	v_lshlrev_b32_e32 v18, 2, v13
	v_add_u32_e32 v11, v4, v9
	v_add_u32_e32 v12, v4, v6
	v_add_u32_e32 v13, v4, v18
	v_and_b32_e32 v4, 0xe0, v0
	v_add_u32_e32 v4, 0x4650, v4
	v_add_u32_e32 v14, v4, v9
	v_add_u32_e32 v16, v4, v6
	v_add_u32_e32 v17, v4, v18
	v_add_u32_e32 v4, -1, v5
	v_max_i32_e32 v19, 0, v4
	v_lshl_add_u32 v19, v19, 5, v7
	v_add_u32_e32 v7, v19, v9
	v_bfe_u32 v2, v0, 3, 2
	v_add_u32_e32 v9, v19, v6
	ds_read_b32 v11, v11
	ds_read_b32 v12, v12
	ds_read_b32 v13, v13
	ds_read_b32 v14, v14
	ds_read_b32 v16, v16
	ds_read_b32 v17, v17
	ds_read_b32 v20, v7
	ds_read_b32 v21, v9
	s_waitcnt lgkmcnt(7)
	v_lshrrev_b32_e32 v7, 2, v11
	s_mov_b32 s26, 0x3ffffffc
	v_and_or_b32 v7, v7, s26, v2
	v_lshlrev_b32_e32 v9, 2, v11
	v_mul_lo_u32 v7, v7, 60
	v_and_b32_e32 v9, 60, v9
	v_add3_u32 v7, v9, v7, 4
	v_or_b32_e32 v9, v10, v15
	v_cmp_gt_u32_e32 vcc, 8, v9
	s_waitcnt lgkmcnt(6)
	v_lshrrev_b32_e32 v9, 2, v12
	v_and_or_b32 v9, v9, s26, v2
	v_lshlrev_b32_e32 v11, 2, v12
	v_mul_lo_u32 v9, v9, 60
	v_and_b32_e32 v11, 60, v11
	v_add3_u32 v9, v11, v9, 8
	s_waitcnt lgkmcnt(5)
	v_lshrrev_b32_e32 v11, 2, v13
	v_and_or_b32 v11, v11, s26, v2
	v_lshlrev_b32_e32 v12, 2, v13
	v_mul_lo_u32 v11, v11, 60
	v_and_b32_e32 v12, 60, v12
	v_or_b32_e32 v10, v10, v3
	v_cndmask_b32_e32 v7, 0, v7, vcc
	v_add3_u32 v11, v12, v11, 12
	v_cmp_gt_u32_e32 vcc, 8, v10
	s_waitcnt lgkmcnt(4)
	v_lshlrev_b32_e32 v12, 2, v14
	v_and_b32_e32 v12, 60, v12
	v_cndmask_b32_e32 v10, 0, v11, vcc
	v_lshrrev_b32_e32 v11, 2, v14
	v_and_or_b32 v11, v11, s26, v2
	v_mul_lo_u32 v11, v11, 60
	s_movk_i32 s4, 0xf4
	v_add3_u32 v11, v11, v12, s4
	v_cmp_eq_u32_e32 vcc, 7, v1
	s_movk_i32 s4, 0xfc
	v_cmp_eq_u32_e64 s[6:7], 7, v5
	v_cndmask_b32_e64 v13, v11, 0, vcc
	s_waitcnt lgkmcnt(3)
	v_lshrrev_b32_e32 v11, 2, v16
	v_and_or_b32 v11, v11, s26, v2
	v_mul_lo_u32 v12, v11, 60
	v_lshlrev_b32_e32 v11, 2, v16
	v_and_b32_e32 v14, 60, v11
	s_waitcnt lgkmcnt(2)
	v_lshrrev_b32_e32 v11, 2, v17
	v_and_or_b32 v11, v11, s26, v2
	v_lshlrev_b32_e32 v16, 2, v17
	v_mul_lo_u32 v11, v11, 60
	v_and_b32_e32 v16, 60, v16
	v_add3_u32 v11, v11, v16, s4
	s_waitcnt lgkmcnt(1)
	v_lshrrev_b32_e32 v16, 2, v20
	v_and_or_b32 v16, v16, s26, v2
	v_lshlrev_b32_e32 v20, 2, v20
	v_cndmask_b32_e64 v9, v9, 0, s[6:7]
	v_cndmask_b32_e64 v17, 2, 1, s[6:7]
	v_mul_lo_u32 v16, v16, 60
	v_and_b32_e32 v20, 60, v20
	s_movk_i32 s6, 0x1e4
	v_or_b32_e32 v15, v4, v15
	v_add3_u32 v16, v16, v20, s6
	v_cmp_gt_u32_e64 s[6:7], 8, v15
	s_waitcnt lgkmcnt(0)
	v_lshlrev_b32_e32 v20, 2, v21
	v_and_b32_e32 v20, 60, v20
	v_cndmask_b32_e64 v15, 0, v16, s[6:7]
	v_lshrrev_b32_e32 v16, 2, v21
	v_and_or_b32 v16, v16, s26, v2
	v_mul_lo_u32 v16, v16, 60
	s_movk_i32 s6, 0x1e8
	v_add_u32_e32 v19, v19, v18
	v_cvt_f32_ubyte0_e32 v18, v2
	v_add3_u32 v16, v16, v20, s6
	v_add_f32_e32 v18, 0.5, v18
	v_mov_b32_e32 v20, -0.5
	v_fmamk_f32 v26, v18, 0x3e800000, v20
	v_cmp_gt_f32_e64 s[8:9], 0, v26
	v_sub_u32_e64 v20, v1, 1 clamp
	v_mov_b32_e32 v22, 0x4750
	v_subbrev_co_u32_e64 v18, s[12:13], 0, v5, s[8:9]
	v_cmp_ngt_f32_e64 s[12:13], 0, v26
	v_max_i32_e32 v18, 0, v18
	v_min_u32_e32 v21, 6, v1
	v_addc_co_u32_e64 v5, s[12:13], 0, v5, s[12:13]
	v_min_u32_e32 v5, 7, v5
	v_lshl_add_u32 v18, v18, 5, v22
	v_lshlrev_b32_e32 v20, 2, v20
	v_lshl_add_u32 v5, v5, 5, v22
	v_add_u32_e32 v23, v18, v20
	v_add_u32_e32 v22, v5, v20
	v_lshlrev_b32_e32 v20, 2, v21
	v_add_u32_e32 v24, v18, v6
	v_add_u32_e32 v6, v5, v6
	v_add_u32_e32 v25, v18, v20
	v_add_u32_e32 v5, v5, v20
	v_lshlrev_b32_e32 v18, 1, v7
	ds_read_b32 v19, v19
	ds_read_b32 v20, v23
	ds_read_b32 v22, v22
	ds_read_b32 v21, v24
	ds_read_b32 v23, v6
	ds_read_b32 v24, v25 offset:4
	ds_read_b32 v25, v5 offset:4
	ds_read_b64 v[6:7], v18
	s_waitcnt lgkmcnt(7)
	v_lshrrev_b32_e32 v5, 2, v19
	v_and_or_b32 v2, v5, s26, v2
	v_lshlrev_b32_e32 v5, 2, v19
	v_cmp_gt_u32_e64 s[6:7], 8, v4
	v_mul_lo_u32 v2, v2, 60
	v_and_b32_e32 v5, 60, v5
	s_movk_i32 s12, 0x1ec
	v_cmp_gt_u32_e64 s[4:5], 8, v3
	v_cndmask_b32_e64 v16, 0, v16, s[6:7]
	v_add3_u32 v2, v2, v5, s12
	v_addc_co_u32_e64 v5, s[6:7], 0, v17, s[6:7]
	v_cndmask_b32_e64 v17, 2, 1, vcc
	v_addc_co_u32_e64 v17, vcc, 0, v17, s[4:5]
	v_mul_u32_u24_e32 v5, v5, v17
	v_cvt_f32_ubyte0_e32 v5, v5
	v_cndmask_b32_e64 v11, 0, v11, s[4:5]
	v_div_scale_f32 v17, s[4:5], v5, v5, 1.0
	v_rcp_f32_e32 v19, v17
	v_or_b32_e32 v3, v4, v3
	v_cmp_gt_u32_e32 vcc, 8, v3
	s_mov_b32 s4, 0x3ec00000
	s_mov_b32 s5, 0x3f600000
	v_cndmask_b32_e32 v30, 0, v2, vcc
	v_fma_f32 v2, -v17, v19, 1.0
	v_fmac_f32_e32 v19, v2, v19
	v_div_scale_f32 v2, vcc, 1.0, v5, 1.0
	v_mul_f32_e32 v3, v2, v19
	v_fma_f32 v4, -v17, v3, v2
	v_fmac_f32_e32 v3, v4, v19
	v_fma_f32 v2, -v17, v3, v2
	v_div_fmas_f32 v2, v2, v19, v3
	v_div_fixup_f32 v4, v2, v5, 1.0
	v_add_f32_e32 v2, 1.0, v26
	v_cndmask_b32_e64 v3, v26, v2, s[8:9]
	v_mov_b32_e32 v26, v3
	v_sub_f32_e32 v2, 1.0, v3
	s_waitcnt lgkmcnt(3)
	v_pk_mul_f32 v[22:23], v[26:27], v[22:23] op_sel_hi:[0,1]
	s_waitcnt lgkmcnt(1)
	v_pk_mul_f32 v[24:25], v[2:3], v[24:25]
	v_pk_fma_f32 v[2:3], v[2:3], v[20:21], v[22:23] op_sel_hi:[0,1,1]
	s_mov_b32 s7, 0x3f200000
	s_mov_b32 s6, 0x3e000000
	v_pk_mul_f32 v[20:21], v[2:3], s[4:5]
	v_pk_mul_f32 v[22:23], v[2:3], s[6:7]
	v_pk_add_f32 v[24:25], v[24:25], v[24:25] op_sel:[0,1] op_sel_hi:[0,1]
	v_pk_fma_f32 v[2:3], v[2:3], s[4:5], v[22:23] op_sel:[0,0,1] op_sel_hi:[1,1,0]
	s_mov_b32 s7, s4
	v_mov_b32_e32 v22, v21
	v_pk_fma_f32 v[20:21], v[24:25], s[6:7], v[22:23]
	s_lshr_b32 s4, s2, 2
	v_lshlrev_b32_e32 v22, 4, v1
	v_lshlrev_b32_e32 v1, 1, v9
	v_lshrrev_b32_e32 v8, 3, v0
	s_and_b32 s4, s4, 0xe0
	s_lshl_b32 s3, s3, 7
	ds_read_b64 v[24:25], v1
	v_or_b32_e32 v8, s4, v8
	s_and_b32 s26, s3, 0x380
	s_movk_i32 s3, 0xf0
	v_pk_mul_f32 v[2:3], v[4:5], v[2:3] op_sel_hi:[0,1]
	v_pk_mul_f32 v[4:5], v[4:5], v[20:21] op_sel_hi:[0,1]
	v_or_b32_e32 v20, s20, v8
	v_lshlrev_b32_e32 v8, 1, v10
	v_add3_u32 v9, v12, v14, s3
	v_lshlrev_b32_e32 v10, 1, v13
	v_lshlrev_b32_e32 v9, 1, v9
	ds_read_b64 v[12:13], v8
	ds_read_b64 v[26:27], v10
	ds_read_b64 v[28:29], v9 offset:16
	s_waitcnt lgkmcnt(3)
	v_pk_add_f16 v6, v6, v24
	v_pk_add_f16 v7, v7, v25
	s_waitcnt lgkmcnt(2)
	v_pk_add_f16 v6, v6, v12
	v_pk_add_f16 v7, v7, v13
	s_waitcnt lgkmcnt(1)
	v_pk_add_f16 v6, v6, v26
	v_pk_add_f16 v7, v7, v27
	v_lshlrev_b32_e32 v12, 1, v11
	s_waitcnt lgkmcnt(0)
	v_pk_add_f16 v19, v7, v29
	v_pk_add_f16 v23, v6, v28
	ds_read_b64 v[6:7], v12
	v_lshlrev_b32_e32 v13, 1, v15
	v_lshlrev_b32_e32 v14, 1, v16
	v_lshlrev_b32_e32 v11, 1, v30
	ds_read_b64 v[16:17], v13
	ds_read_b64 v[24:25], v14
	ds_read_b64 v[26:27], v11
	s_waitcnt lgkmcnt(3)
	v_pk_add_f16 v6, v23, v6
	v_pk_add_f16 v7, v19, v7
	s_load_dwordx2 s[24:25], s[0:1], 0x30
	s_waitcnt lgkmcnt(0)
	v_pk_add_f16 v7, v7, v17
	v_pk_add_f16 v6, v6, v16
	v_pk_add_f16 v7, v7, v25
	v_pk_add_f16 v6, v6, v24
	v_pk_add_f16 v7, v7, v27
	v_pk_add_f16 v6, v6, v26
	v_mov_b32_e32 v21, s21
	v_cvt_f32_f16_e32 v16, v6
	v_cvt_f32_f16_sdwa v17, v6 dst_sel:DWORD dst_unused:UNUSED_PAD src0_sel:WORD_1
	v_cvt_f32_f16_e32 v24, v7
	v_cvt_f32_f16_sdwa v25, v7 dst_sel:DWORD dst_unused:UNUSED_PAD src0_sel:WORD_1
	v_lshlrev_b64 v[20:21], 10, v[20:21]
	s_mov_b32 s27, 0
	v_lshl_add_u64 v[20:21], s[24:25], 0, v[20:21]
	v_lshl_add_u64 v[20:21], v[20:21], 0, s[26:27]
	v_mov_b32_e32 v23, 0
	s_movk_i32 s3, 0x100
	v_lshl_add_u64 v[6:7], v[20:21], 0, v[22:23]
	v_pk_mul_f32 v[20:21], v[2:3], v[16:17]
	v_pk_mul_f32 v[22:23], v[4:5], v[24:25]
	v_cmp_gt_u32_e32 vcc, s3, v0
	global_store_dwordx4 v[6:7], v[20:23], off nt
	s_and_b64 exec, exec, vcc
	s_cbranch_execz .LBB3_13
	ds_read_b64 v[16:17], v18 offset:7208
	ds_read_b64 v[18:19], v1 offset:7208
	ds_read_b64 v[20:21], v8 offset:7208
	ds_read_b64 v[22:23], v10 offset:7208
	v_add_co_u32_e32 v6, vcc, 0x40000, v6
	s_waitcnt lgkmcnt(2)
	v_pk_add_f16 v8, v17, v19
	v_pk_add_f16 v1, v16, v18
	s_waitcnt lgkmcnt(1)
	v_pk_add_f16 v10, v8, v21
	ds_read_b64 v[8:9], v9 offset:7224
	ds_read_b64 v[16:17], v12 offset:7208
	ds_read_b64 v[12:13], v13 offset:7208
	ds_read_b64 v[14:15], v14 offset:7208
	v_pk_add_f16 v1, v1, v20
	s_waitcnt lgkmcnt(4)
	v_pk_add_f16 v10, v10, v23
	v_pk_add_f16 v1, v1, v22
	s_waitcnt lgkmcnt(3)
	v_pk_add_f16 v9, v10, v9
	v_pk_add_f16 v1, v1, v8
	s_waitcnt lgkmcnt(2)
	v_pk_add_f16 v10, v9, v17
	ds_read_b64 v[8:9], v11 offset:7208
	v_pk_add_f16 v1, v1, v16
	s_waitcnt lgkmcnt(2)
	v_pk_add_f16 v10, v10, v13
	v_pk_add_f16 v1, v1, v12
	s_waitcnt lgkmcnt(1)
	v_pk_add_f16 v10, v10, v15
	v_pk_add_f16 v1, v1, v14
	s_waitcnt lgkmcnt(0)
	v_pk_add_f16 v11, v10, v9
	v_pk_add_f16 v1, v1, v8
	v_cvt_f32_f16_e32 v10, v11
	v_cvt_f32_f16_e32 v8, v1
	v_cvt_f32_f16_sdwa v9, v1 dst_sel:DWORD dst_unused:UNUSED_PAD src0_sel:WORD_1
	v_cvt_f32_f16_sdwa v11, v11 dst_sel:DWORD dst_unused:UNUSED_PAD src0_sel:WORD_1
	v_addc_co_u32_e32 v7, vcc, 0, v7, vcc
	v_pk_mul_f32 v[2:3], v[2:3], v[8:9]
	v_pk_mul_f32 v[4:5], v[4:5], v[10:11]
	global_store_dwordx4 v[6:7], v[2:5], off nt

	.amdhsa_kernel _Z10k_transferPKtS0_PKfPKiS2_S4_PfS5_S5_
		.amdhsa_group_segment_fixed_size 18512
		.amdhsa_private_segment_fixed_size 0
		.amdhsa_kernarg_size 72
		.amdhsa_user_sgpr_count 2
		.amdhsa_user_sgpr_dispatch_ptr 0
		.amdhsa_user_sgpr_queue_ptr 0
		.amdhsa_user_sgpr_kernarg_segment_ptr 1
		.amdhsa_user_sgpr_dispatch_id 0
		.amdhsa_user_sgpr_kernarg_preload_length 0
		.amdhsa_user_sgpr_kernarg_preload_offset 0
		.amdhsa_user_sgpr_private_segment_size 0
		.amdhsa_uses_dynamic_stack 0
		.amdhsa_enable_private_segment 0
		.amdhsa_system_sgpr_workgroup_id_x 1
		.amdhsa_system_sgpr_workgroup_id_y 0
		.amdhsa_system_sgpr_workgroup_id_z 0
		.amdhsa_system_sgpr_workgroup_info 0
		.amdhsa_system_vgpr_workitem_id 0
		.amdhsa_next_free_vgpr 52
		.amdhsa_next_free_sgpr 28
		.amdhsa_accum_offset 52
		.amdhsa_reserve_vcc 1
		.amdhsa_float_round_mode_32 0
		.amdhsa_float_round_mode_16_64 0
		.amdhsa_float_denorm_mode_32 3
		.amdhsa_float_denorm_mode_16_64 3
		.amdhsa_dx10_clamp 1
		.amdhsa_ieee_mode 1
		.amdhsa_fp16_overflow 0
		.amdhsa_tg_split 0
		.amdhsa_exception_fp_ieee_invalid_op 0
		.amdhsa_exception_fp_denorm_src 0
		.amdhsa_exception_fp_ieee_div_zero 0
		.amdhsa_exception_fp_ieee_overflow 0
		.amdhsa_exception_fp_ieee_underflow 0
		.amdhsa_exception_fp_ieee_inexact 0
		.amdhsa_exception_int_div_zero 0
	.end_amdhsa_kernel

amdhsa.kernels:
  - .agpr_count:     0
    .args:
      - .actual_access:  read_only
        .address_space:  global
        .offset:         0
        .size:           8
        .value_kind:     global_buffer
      - .actual_access:  read_only
        .address_space:  global
        .offset:         8
        .size:           8
        .value_kind:     global_buffer
      - .actual_access:  write_only
        .address_space:  global
        .offset:         16
        .size:           8
        .value_kind:     global_buffer
      - .actual_access:  write_only
        .address_space:  global
        .offset:         24
        .size:           8
        .value_kind:     global_buffer
      - .actual_access:  write_only
        .address_space:  global
        .offset:         32
        .size:           8
        .value_kind:     global_buffer
      - .actual_access:  write_only
        .address_space:  global
        .offset:         40
        .size:           8
        .value_kind:     global_buffer
      - .actual_access:  write_only
        .address_space:  global
        .offset:         48
        .size:           8
        .value_kind:     global_buffer
      - .actual_access:  write_only
        .address_space:  global
        .offset:         56
        .size:           8
        .value_kind:     global_buffer
      - .actual_access:  write_only
        .address_space:  global
        .offset:         64
        .size:           8
        .value_kind:     global_buffer
    .group_segment_fixed_size: 18944
    .kernarg_segment_align: 8
    .kernarg_segment_size: 72
    .language:       OpenCL C
    .language_version:
      - 2
      - 0
    .max_flat_workgroup_size: 256
    .name:           _Z6k_prepPKfS0_PfS1_PdS2_PtS3_S3_
    .private_segment_fixed_size: 0
    .sgpr_count:     34
    .sgpr_spill_count: 0
    .symbol:         _Z6k_prepPKfS0_PfS1_PdS2_PtS3_S3_.kd
    .uniform_work_group_size: 1
    .uses_dynamic_stack: false
    .vgpr_count:     29
    .vgpr_spill_count: 0
    .wavefront_size: 64
  - .agpr_count:     16
    .args:
      - .actual_access:  read_only
        .address_space:  global
        .offset:         0
        .size:           8
        .value_kind:     global_buffer
      - .actual_access:  read_only
        .address_space:  global
        .offset:         8
        .size:           8
        .value_kind:     global_buffer
      - .actual_access:  read_only
        .address_space:  global
        .offset:         16
        .size:           8
        .value_kind:     global_buffer
      - .actual_access:  read_only
        .address_space:  global
        .offset:         24
        .size:           8
        .value_kind:     global_buffer
      - .actual_access:  write_only
        .address_space:  global
        .offset:         32
        .size:           8
        .value_kind:     global_buffer
    .group_segment_fixed_size: 256
    .kernarg_segment_align: 8
    .kernarg_segment_size: 40
    .language:       OpenCL C
    .language_version:
      - 2
      - 0
    .max_flat_workgroup_size: 256
    .name:           _Z9k_coarse2PKtS0_PKdS2_Pf
    .private_segment_fixed_size: 0
    .sgpr_count:     37
    .sgpr_spill_count: 0
    .symbol:         _Z9k_coarse2PKtS0_PKdS2_Pf.kd
    .uniform_work_group_size: 1
    .uses_dynamic_stack: false
    .vgpr_count:     156
    .vgpr_spill_count: 0
    .wavefront_size: 64
  - .agpr_count:     0
    .args:
      - .actual_access:  read_only
        .address_space:  global
        .offset:         0
        .size:           8
        .value_kind:     global_buffer
      - .actual_access:  read_only
        .address_space:  global
        .offset:         8
        .size:           8
        .value_kind:     global_buffer
      - .actual_access:  read_only
        .address_space:  global
        .offset:         16
        .size:           8
        .value_kind:     global_buffer
      - .actual_access:  read_only
        .address_space:  global
        .offset:         24
        .size:           8
        .value_kind:     global_buffer
      - .actual_access:  read_only
        .address_space:  global
        .offset:         32
        .size:           8
        .value_kind:     global_buffer
      - .actual_access:  read_only
        .address_space:  global
        .offset:         40
        .size:           8
        .value_kind:     global_buffer
      - .actual_access:  read_only
        .address_space:  global
        .offset:         48
        .size:           8
        .value_kind:     global_buffer
      - .actual_access:  write_only
        .address_space:  global
        .offset:         56
        .size:           8
        .value_kind:     global_buffer
      - .actual_access:  write_only
        .address_space:  global
        .offset:         64
        .size:           8
        .value_kind:     global_buffer
      - .actual_access:  write_only
        .address_space:  global
        .offset:         72
        .size:           8
        .value_kind:     global_buffer
      - .actual_access:  read_only
        .address_space:  global
        .offset:         80
        .size:           8
        .value_kind:     global_buffer
      - .actual_access:  read_only
        .address_space:  global
        .offset:         88
        .size:           8
        .value_kind:     global_buffer
      - .actual_access:  write_only
        .address_space:  global
        .offset:         96
        .size:           8
        .value_kind:     global_buffer
      - .actual_access:  write_only
        .address_space:  global
        .offset:         104
        .size:           8
        .value_kind:     global_buffer
    .group_segment_fixed_size: 30768
    .kernarg_segment_align: 8
    .kernarg_segment_size: 112
    .language:       OpenCL C
    .language_version:
      - 2
      - 0
    .max_flat_workgroup_size: 512
    .name:           _Z7k_fine3PKfS0_PKtS2_PKdS4_S0_PiPfS5_S0_S0_PtS7_
    .private_segment_fixed_size: 0
    .sgpr_count:     106
    .sgpr_spill_count: 4
    .symbol:         _Z7k_fine3PKfS0_PKtS2_PKdS4_S0_PiPfS5_S0_S0_PtS7_.kd
    .uniform_work_group_size: 1
    .uses_dynamic_stack: false
    .vgpr_count:     256
    .vgpr_spill_count: 0
    .wavefront_size: 64
  - .agpr_count:     0
    .args:
      - .actual_access:  read_only
        .address_space:  global
        .offset:         0
        .size:           8
        .value_kind:     global_buffer
      - .actual_access:  read_only
        .address_space:  global
        .offset:         8
        .size:           8
        .value_kind:     global_buffer
      - .actual_access:  read_only
        .address_space:  global
        .offset:         16
        .size:           8
        .value_kind:     global_buffer
      - .actual_access:  read_only
        .address_space:  global
        .offset:         24
        .size:           8
        .value_kind:     global_buffer
      - .actual_access:  read_only
        .address_space:  global
        .offset:         32
        .size:           8
        .value_kind:     global_buffer
      - .actual_access:  read_only
        .address_space:  global
        .offset:         40
        .size:           8
        .value_kind:     global_buffer
      - .actual_access:  write_only
        .address_space:  global
        .offset:         48
        .size:           8
        .value_kind:     global_buffer
      - .actual_access:  write_only
        .address_space:  global
        .offset:         56
        .size:           8
        .value_kind:     global_buffer
      - .actual_access:  write_only
        .address_space:  global
        .offset:         64
        .size:           8
        .value_kind:     global_buffer
    .group_segment_fixed_size: 18512
    .kernarg_segment_align: 8
    .kernarg_segment_size: 72
    .language:       OpenCL C
    .language_version:
      - 2
      - 0
    .max_flat_workgroup_size: 256
    .name:           _Z10k_transferPKtS0_PKfPKiS2_S4_PfS5_S5_
    .private_segment_fixed_size: 0
    .sgpr_count:     34
    .sgpr_spill_count: 0
    .symbol:         _Z10k_transferPKtS0_PKfPKiS2_S4_PfS5_S5_.kd
    .uniform_work_group_size: 1
    .uses_dynamic_stack: false
    .vgpr_count:     52
    .vgpr_spill_count: 0
    .wavefront_size: 64
